# P8 unit-top drain -> counted wait at first use; P17 final pass slot words preloaded (as P18)
# baseline (speedup 1.0000x reference)
.LBB0_1262:
	s_mul_hi_i32 s20, s80, 0x66666667
	s_lshr_b32 s48, s20, 31
	s_ashr_i32 s20, s20, 2
	s_add_i32 s20, s20, s48
	s_mul_i32 s48, s20, 0xfffffb00
	s_add_i32 s48, s48, s35
	s_waitcnt lgkmcnt(0)
	v_add_u32_e32 v2, s48, v158
	v_ashrrev_i32_e32 v3, 31, v2
	v_lshlrev_b64 v[2:3], 2, v[2:3]
	v_lshl_add_u64 v[6:7], s[62:63], 0, v[2:3]
	v_add_co_u32_e32 v4, vcc, s3, v6
	global_load_dwordx4 v[58:61], v[6:7], off
	s_nop 0
	v_addc_co_u32_e32 v5, vcc, 0, v7, vcc
	global_load_dwordx4 v[94:97], v[4:5], off offset:1024
	v_lshl_add_u64 v[2:3], s[64:65], 0, v[2:3]
	global_load_dwordx4 v[70:73], v[2:3], off
	v_lshl_add_u64 v[4:5], v[6:7], 0, s[38:39]
	global_load_dwordx4 v[98:101], v[4:5], off offset:16
	global_load_dwordx4 v[62:65], v[6:7], off offset:16
	global_load_dwordx4 v[66:69], v[2:3], off offset:16
	s_mul_i32 s52, s20, 0xffffffec
	v_add_co_u32_e32 v2, vcc, s29, v6
	s_add_i32 s52, s33, s52
	s_nop 0
	v_addc_co_u32_e32 v3, vcc, 0, v7, vcc
	s_ashr_i32 s53, s52, 31
	v_add_co_u32_e32 v4, vcc, s47, v6
	s_lshl_b64 s[54:55], s[52:53], 16
	s_nop 0
	v_addc_co_u32_e32 v5, vcc, 0, v7, vcc
	v_lshl_add_u64 v[8:9], v[156:157], 0, s[54:55]
	global_load_dwordx4 v[102:105], v[4:5], off offset:3072
	global_load_dwordx4 v[86:89], v[2:3], off offset:2048
	global_load_dwordx4 v[42:45], v[8:9], off
	global_load_dwordx4 v[26:29], v[8:9], off offset:1024
	global_load_dwordx4 v[10:13], v[8:9], off offset:2048
	s_nop 0
	global_load_dwordx4 v[2:5], v[8:9], off offset:3072
	v_add_co_u32_e32 v22, vcc, s3, v8
	v_lshlrev_b32_e32 v111, 16, v201
	s_nop 0
	v_addc_co_u32_e32 v23, vcc, 0, v9, vcc
	v_add_co_u32_e32 v24, vcc, s29, v8
	v_lshlrev_b32_e32 v110, 16, v206
	s_nop 0
	v_addc_co_u32_e32 v25, vcc, 0, v9, vcc
	v_add_co_u32_e32 v82, vcc, s47, v8
	global_load_dwordx4 v[30:33], v[22:23], off offset:1024
	global_load_dwordx4 v[14:17], v[22:23], off offset:2048
	global_load_dwordx4 v[46:49], v[24:25], off offset:-4096
	global_load_dwordx4 v[50:53], v[24:25], off
	global_load_dwordx4 v[34:37], v[24:25], off offset:1024
	global_load_dwordx4 v[18:21], v[24:25], off offset:2048
	v_addc_co_u32_e32 v83, vcc, 0, v9, vcc
	v_lshl_add_u64 v[8:9], v[6:7], 0, s[40:41]
	v_lshl_add_u64 v[6:7], v[6:7], 0, s[42:43]
	global_load_dwordx4 v[106:109], v[6:7], off offset:16
	global_load_dwordx4 v[74:77], v[8:9], off offset:16
	global_load_dwordx4 v[78:81], v[24:25], off offset:3072
	s_nop 0
	global_load_dwordx4 v[6:9], v[22:23], off offset:3072
	global_load_dwordx4 v[54:57], v[82:83], off
	global_load_dwordx4 v[38:41], v[82:83], off offset:1024
	s_nop 0
	global_load_dwordx4 v[22:25], v[82:83], off offset:2048
	s_nop 0
	global_load_dwordx4 v[82:85], v[82:83], off offset:3072
	v_lshlrev_b32_e32 v114, 16, v207
	v_lshlrev_b32_e32 v115, 16, v202
	v_and_b32_e32 v117, 0xffff0000, v202
	v_and_b32_e32 v116, 0xffff0000, v207
	v_and_b32_e32 v113, 0xffff0000, v201
	v_and_b32_e32 v112, 0xffff0000, v206
	v_and_b32_e32 v121, 0xffff0000, v203
	v_and_b32_e32 v120, 0xffff0000, v209
	v_lshlrev_b32_e32 v122, 16, v210
	v_lshlrev_b32_e32 v123, 16, v205
	v_and_b32_e32 v125, 0xffff0000, v205
	v_and_b32_e32 v124, 0xffff0000, v210
	v_lshlrev_b32_e32 v127, 16, v212
	v_lshlrev_b32_e32 v126, 16, v218
	v_and_b32_e32 v129, 0xffff0000, v212
	v_and_b32_e32 v128, 0xffff0000, v218
	v_lshlrev_b32_e32 v131, 16, v213
	v_and_b32_e32 v133, 0xffff0000, v213
	v_and_b32_e32 v132, 0xffff0000, v219
	v_lshlrev_b32_e32 v135, 16, v215
	v_and_b32_e32 v137, 0xffff0000, v215
	v_and_b32_e32 v136, 0xffff0000, v221
	v_lshlrev_b32_e32 v139, 16, v216
	v_and_b32_e32 v141, 0xffff0000, v216
	v_and_b32_e32 v140, 0xffff0000, v222
	s_and_b32 s49, s79, 0x8000
	s_add_i32 s49, s49, 0
	v_add3_u32 v147, s49, v186, v187
	s_add_i32 s53, s31, s49
	s_add_i32 s52, s52, 1
	v_add_u32_e32 v245, s49, v165
	s_waitcnt vmcnt(14)
	v_mov_b32_e32 v93, v58
	v_mov_b32_e32 v91, v60
	v_mov_b32_e32 v92, v94
	v_mov_b32_e32 v58, v95
	v_mov_b32_e32 v90, v96
	v_mov_b32_e32 v60, v97
	v_fma_f32 v95, v93, v111, v70
	v_pk_mul_f32 v[118:119], v[90:91], v[114:115]
	v_fma_f32 v115, v92, v110, v95
	v_add_f32_e32 v111, v119, v72
	v_fma_f32 v95, v61, v117, v73
	v_fma_f32 v97, v59, v113, v71
	v_add_f32_e32 v111, v118, v111
	v_fma_f32 v134, v60, v116, v95
	v_lshlrev_b32_e32 v119, 16, v203
	v_lshlrev_b32_e32 v118, 16, v209
	v_mov_b32_e32 v94, v98
	v_mov_b32_e32 v95, v62
	v_fma_f32 v130, v58, v112, v97
	s_nop 0
	v_fma_f32 v62, v95, v119, v66
	v_fma_f32 v119, v94, v118, v62
	v_mov_b32_e32 v62, v99
	s_nop 0
	v_fma_f32 v97, v63, v121, v67
	v_fma_f32 v138, v62, v120, v97
	v_mov_b32_e32 v96, v100
	v_mov_b32_e32 v97, v64
	s_nop 0
	v_fma_f32 v64, v97, v123, v68
	v_fma_f32 v123, v96, v122, v64
	v_mov_b32_e32 v64, v101
	s_nop 0
	v_fma_f32 v99, v65, v125, v69
	v_fma_f32 v142, v64, v124, v99
	v_mov_b32_e32 v98, v102
	v_mov_b32_e32 v99, v86
	s_nop 0
	v_fma_f32 v86, v99, v127, v115
	v_fma_f32 v115, v98, v126, v86
	v_mov_b32_e32 v86, v103
	s_nop 0
	v_fma_f32 v101, v87, v129, v130
	v_fma_f32 v143, v86, v128, v101
	v_lshlrev_b32_e32 v130, 16, v219
	v_mov_b32_e32 v100, v104
	v_mov_b32_e32 v101, v88
	s_nop 0
	v_fma_f32 v88, v101, v131, v111
	v_fma_f32 v111, v100, v130, v88
	v_mov_b32_e32 v88, v105
	s_nop 0
	v_fma_f32 v103, v89, v133, v134
	v_fma_f32 v144, v88, v132, v103
	v_lshlrev_b32_e32 v134, 16, v221
	s_waitcnt vmcnt(7)
	v_mov_b32_e32 v102, v106
	s_waitcnt vmcnt(6)
	v_mov_b32_e32 v103, v74
	s_nop 0
	v_fma_f32 v74, v103, v135, v119
	v_fma_f32 v119, v102, v134, v74
	v_mov_b32_e32 v74, v107
	s_nop 0
	v_fma_f32 v105, v75, v137, v138
	v_fma_f32 v145, v74, v136, v105
	v_lshlrev_b32_e32 v138, 16, v222
	v_mov_b32_e32 v104, v108
	v_mov_b32_e32 v105, v76
	s_nop 0
	v_fma_f32 v76, v105, v139, v123
	v_fma_f32 v123, v104, v138, v76
	v_mov_b32_e32 v76, v109
	s_nop 0
	v_fma_f32 v107, v77, v141, v142
	v_fma_f32 v109, v76, v140, v107
	v_cvt_pk_bf16_f32 v106, v115, v143
	v_cvt_pk_bf16_f32 v107, v111, v144
	v_add3_u32 v111, s49, v184, v185
	v_cvt_pk_bf16_f32 v108, v119, v145
	v_cvt_pk_bf16_f32 v109, v123, v109
	ds_write_b128 v111, v[106:109]
	v_pk_mov_b32 v[106:107], v[126:127], v[110:111] op_sel:[1,0]
	v_lshlrev_b32_e32 v111, 16, v224
	v_lshlrev_b32_e32 v110, 16, v228
	v_fma_f32 v107, v93, v107, v70
	v_fma_f32 v108, v92, v106, v107
	v_pk_mov_b32 v[106:107], v[128:129], v[112:113] op_sel:[1,0]
	v_pk_mov_b32 v[112:113], v[110:111], v[126:127] op_sel:[1,0]
	s_nop 0
	v_fma_f32 v107, v59, v107, v71
	v_fma_f32 v109, v58, v106, v107
	v_pk_mov_b32 v[106:107], v[130:131], v[114:115] op_sel:[1,0]
	v_and_b32_e32 v115, 0xffff0000, v224
	s_nop 0
	v_fma_f32 v107, v91, v107, v72
	v_fma_f32 v123, v90, v106, v107
	v_pk_mov_b32 v[106:107], v[132:133], v[116:117] op_sel:[1,0]
	s_nop 0
	s_nop 0
	v_fma_f32 v107, v61, v107, v73
	v_fma_f32 v142, v60, v106, v107
	v_pk_mov_b32 v[106:107], v[134:135], v[118:119] op_sel:[1,0]
	s_nop 0
	s_nop 0
	v_fma_f32 v107, v95, v107, v66
	v_fma_f32 v143, v94, v106, v107
	v_pk_mov_b32 v[106:107], v[136:137], v[120:121] op_sel:[1,0]
	s_nop 0
	s_nop 0
	v_fma_f32 v107, v63, v107, v67
	v_fma_f32 v144, v62, v106, v107
	v_pk_mov_b32 v[106:107], v[138:139], v[122:123] op_sel:[1,0]
	s_nop 0
	s_nop 0
	v_fma_f32 v107, v97, v107, v68
	v_fma_f32 v145, v96, v106, v107
	v_pk_mov_b32 v[106:107], v[140:141], v[124:125] op_sel:[1,0]
	s_nop 0
	s_nop 0
	v_fma_f32 v107, v65, v107, v69
	v_fma_f32 v146, v64, v106, v107
	v_pk_mul_f32 v[106:107], v[92:93], v[126:127]
	v_lshlrev_b32_e32 v127, 16, v226
	v_add_f32_e32 v107, v107, v70
	v_add_f32_e32 v114, v106, v107
	v_pk_mul_f32 v[92:93], v[92:93], v[112:113]
	v_fma_f32 v107, v59, v129, v71
	v_fma_f32 v118, v58, v128, v107
	v_add_f32_e32 v70, v93, v70
	v_fma_f32 v107, v91, v131, v72
	v_fma_f32 v122, v90, v130, v107
	v_add_f32_e32 v70, v92, v70
	v_fma_f32 v107, v61, v133, v73
	v_fma_f32 v148, v60, v132, v107
	s_nop 0
	v_fma_f32 v107, v95, v135, v66
	v_fma_f32 v149, v94, v134, v107
	s_nop 0
	v_fma_f32 v107, v63, v137, v67
	v_fma_f32 v150, v62, v136, v107
	s_nop 0
	v_fma_f32 v107, v97, v139, v68
	v_fma_f32 v151, v96, v138, v107
	s_nop 0
	v_fma_f32 v107, v65, v141, v69
	v_fma_f32 v152, v64, v140, v107
	s_nop 0
	v_fma_f32 v107, v99, v113, v108
	v_fma_f32 v119, v98, v112, v107
	s_nop 0
	v_fma_f32 v107, v99, v111, v114
	v_and_b32_e32 v114, 0xffff0000, v228
	v_pk_mov_b32 v[116:117], v[114:115], v[128:129] op_sel:[1,0]
	v_fma_f32 v111, v98, v110, v107
	v_pk_mul_f32 v[58:59], v[58:59], v[116:117]
	v_fma_f32 v107, v87, v117, v109
	v_fma_f32 v106, v86, v116, v107
	v_cvt_pk_bf16_f32 v106, v119, v106
	v_lshlrev_b32_e32 v119, 16, v225
	v_fma_f32 v107, v87, v115, v118
	v_lshlrev_b32_e32 v118, 16, v229
	v_pk_mov_b32 v[120:121], v[118:119], v[130:131] op_sel:[1,0]
	v_fma_f32 v115, v86, v114, v107
	v_and_b32_e32 v131, 0xffff0000, v226
	v_fma_f32 v107, v101, v121, v123
	v_fma_f32 v107, v100, v120, v107
	v_and_b32_e32 v123, 0xffff0000, v225
	v_fma_f32 v109, v101, v119, v122
	v_and_b32_e32 v122, 0xffff0000, v229
	v_pk_mov_b32 v[124:125], v[122:123], v[132:133] op_sel:[1,0]
	v_fma_f32 v119, v100, v118, v109
	v_and_b32_e32 v130, 0xffff0000, v230
	v_fma_f32 v109, v89, v125, v142
	v_fma_f32 v126, v88, v124, v109
	v_cvt_pk_bf16_f32 v107, v107, v126
	v_lshlrev_b32_e32 v126, 16, v230
	v_fma_f32 v109, v89, v123, v148
	v_pk_mov_b32 v[128:129], v[126:127], v[134:135] op_sel:[1,0]
	v_fma_f32 v123, v88, v122, v109
	v_pk_mov_b32 v[132:133], v[130:131], v[136:137] op_sel:[1,0]
	v_fma_f32 v109, v103, v129, v143
	v_fma_f32 v142, v102, v128, v109
	v_add_f32_e32 v59, v59, v71
	v_fma_f32 v109, v103, v127, v149
	v_fma_f32 v127, v102, v126, v109
	v_fma_f32 v109, v75, v133, v144
	v_add_f32_e32 v71, v58, v59
	v_fma_f32 v108, v74, v132, v109
	v_fma_f32 v109, v75, v131, v150
	v_fma_f32 v59, v91, v121, v72
	v_fma_f32 v131, v74, v130, v109
	v_lshlrev_b32_e32 v134, 16, v231
	v_lshlrev_b32_e32 v135, 16, v227
	v_fma_f32 v72, v90, v120, v59
	v_pk_mov_b32 v[136:137], v[134:135], v[138:139] op_sel:[1,0]
	v_fma_f32 v59, v61, v125, v73
	v_fma_f32 v60, v60, v124, v59
	v_fma_f32 v109, v105, v137, v145
	v_fma_f32 v59, v95, v129, v66
	v_fma_f32 v109, v104, v136, v109
	v_fma_f32 v61, v94, v128, v59
	v_fma_f32 v135, v105, v135, v151
	v_fma_f32 v59, v63, v133, v67
	v_fma_f32 v135, v104, v134, v135
	v_and_b32_e32 v139, 0xffff0000, v227
	v_and_b32_e32 v138, 0xffff0000, v231
	v_fma_f32 v62, v62, v132, v59
	v_pk_mov_b32 v[140:141], v[138:139], v[140:141] op_sel:[1,0]
	v_fma_f32 v59, v97, v137, v68
	v_fma_f32 v63, v96, v136, v59
	v_cvt_pk_bf16_f32 v108, v142, v108
	v_fma_f32 v59, v65, v141, v69
	v_fma_f32 v64, v64, v140, v59
	v_lshlrev_b32_e32 v58, 16, v232
	v_mov_b32_e32 v59, v110
	v_fma_f32 v143, v77, v141, v146
	v_fma_f32 v59, v99, v59, v70
	v_fma_f32 v65, v98, v58, v59
	v_and_b32_e32 v58, 0xffff0000, v232
	v_mov_b32_e32 v59, v114
	v_fma_f32 v144, v76, v140, v143
	v_fma_f32 v59, v87, v59, v71
	v_fma_f32 v66, v86, v58, v59
	v_lshlrev_b32_e32 v58, 16, v233
	v_mov_b32_e32 v59, v118
	v_pk_mul_f32 v[142:143], v[76:77], v[138:139]
	v_fma_f32 v59, v101, v59, v72
	v_fma_f32 v67, v100, v58, v59
	v_and_b32_e32 v58, 0xffff0000, v233
	v_mov_b32_e32 v59, v122
	v_add_f32_e32 v139, v143, v152
	v_fma_f32 v59, v89, v59, v60
	v_fma_f32 v60, v88, v58, v59
	v_lshlrev_b32_e32 v58, 16, v234
	v_mov_b32_e32 v59, v126
	v_cvt_pk_bf16_f32 v109, v109, v144
	ds_write_b128 v147, v[106:109]
	v_fma_f32 v59, v103, v59, v61
	v_fma_f32 v61, v102, v58, v59
	v_and_b32_e32 v58, 0xffff0000, v234
	v_mov_b32_e32 v59, v130
	v_add_f32_e32 v109, v142, v139
	v_fma_f32 v59, v75, v59, v62
	v_fma_f32 v62, v74, v58, v59
	v_lshlrev_b32_e32 v58, 16, v235
	v_mov_b32_e32 v59, v134
	v_cvt_pk_bf16_f32 v106, v111, v115
	v_add3_u32 v111, s49, v188, v189
	v_fma_f32 v59, v105, v59, v63
	v_fma_f32 v63, v104, v58, v59
	v_and_b32_e32 v58, 0xffff0000, v235
	v_mov_b32_e32 v59, v138
	v_cvt_pk_bf16_f32 v107, v119, v123
	v_cvt_pk_bf16_f32 v108, v127, v131
	v_cvt_pk_bf16_f32 v109, v135, v109
	ds_write_b128 v111, v[106:109]
	v_fma_f32 v59, v77, v59, v64
	v_fma_f32 v64, v76, v58, v59
	v_cvt_pk_bf16_f32 v58, v65, v66
	v_cvt_pk_bf16_f32 v59, v67, v60
	v_cvt_pk_bf16_f32 v60, v61, v62
	v_add3_u32 v62, s49, v190, v191
	v_cvt_pk_bf16_f32 v61, v63, v64
	ds_write_b128 v62, v[58:61]
	v_add_u32_e32 v58, s53, v192
	v_add_u32_e32 v242, v58, v193
	s_waitcnt lgkmcnt(0)
	s_barrier
	ds_read_b128 v[58:61], v242
	ds_read_b128 v[62:65], v242 offset:4096
	ds_read_b128 v[98:101], v242 offset:8192
	ds_read_b128 v[102:105], v242 offset:12288
	s_waitcnt lgkmcnt(3)
	v_mfma_f32_16x16x32_bf16 v[66:69], v[42:45], v[58:61], 0
	v_mfma_f32_16x16x32_bf16 v[70:73], v[46:49], v[58:61], 0
	v_mfma_f32_16x16x32_bf16 v[74:77], v[50:53], v[58:61], 0
	s_waitcnt vmcnt(3)
	v_mfma_f32_16x16x32_bf16 v[58:61], v[54:57], v[58:61], 0
	s_waitcnt lgkmcnt(2)
	v_mfma_f32_16x16x32_bf16 v[86:89], v[42:45], v[62:65], 0
	v_mfma_f32_16x16x32_bf16 v[90:93], v[46:49], v[62:65], 0
	v_mfma_f32_16x16x32_bf16 v[94:97], v[50:53], v[62:65], 0
	v_mfma_f32_16x16x32_bf16 v[62:65], v[54:57], v[62:65], 0
	s_waitcnt lgkmcnt(1)
	v_mfma_f32_16x16x32_bf16 v[106:109], v[42:45], v[98:101], 0
	v_mfma_f32_16x16x32_bf16 v[110:113], v[46:49], v[98:101], 0
	v_mfma_f32_16x16x32_bf16 v[114:117], v[50:53], v[98:101], 0
	v_mfma_f32_16x16x32_bf16 v[98:101], v[54:57], v[98:101], 0
	s_waitcnt lgkmcnt(0)
	v_mfma_f32_16x16x32_bf16 v[42:45], v[42:45], v[102:105], 0
	v_mfma_f32_16x16x32_bf16 v[46:49], v[46:49], v[102:105], 0
	v_mfma_f32_16x16x32_bf16 v[50:53], v[50:53], v[102:105], 0
	v_mfma_f32_16x16x32_bf16 v[54:57], v[54:57], v[102:105], 0
	v_add_u32_e32 v102, s53, v194
	v_add_u32_e32 v243, v102, v193
	ds_read_b128 v[102:105], v243
	ds_read_b128 v[118:121], v243 offset:4096
	s_waitcnt lgkmcnt(1)
	v_mfma_f32_16x16x32_bf16 v[66:69], v[26:29], v[102:105], v[66:69]
	v_mfma_f32_16x16x32_bf16 v[70:73], v[30:33], v[102:105], v[70:73]
	v_mfma_f32_16x16x32_bf16 v[74:77], v[34:37], v[102:105], v[74:77]
	s_waitcnt vmcnt(2)
	v_mfma_f32_16x16x32_bf16 v[58:61], v[38:41], v[102:105], v[58:61]
	s_waitcnt lgkmcnt(0)
	v_mfma_f32_16x16x32_bf16 v[86:89], v[26:29], v[118:121], v[86:89]
	v_mfma_f32_16x16x32_bf16 v[90:93], v[30:33], v[118:121], v[90:93]
	v_mfma_f32_16x16x32_bf16 v[94:97], v[34:37], v[118:121], v[94:97]
	v_mfma_f32_16x16x32_bf16 v[62:65], v[38:41], v[118:121], v[62:65]
	ds_read_b128 v[102:105], v243 offset:8192
	ds_read_b128 v[118:121], v243 offset:12288
	s_waitcnt lgkmcnt(1)
	v_mfma_f32_16x16x32_bf16 v[106:109], v[26:29], v[102:105], v[106:109]
	s_waitcnt lgkmcnt(0)
	v_mfma_f32_16x16x32_bf16 v[26:29], v[26:29], v[118:121], v[42:45]
	s_nop 2
	v_add_u32_e32 v42, s53, v195
	v_add_u32_e32 v244, v42, v193
	v_mfma_f32_16x16x32_bf16 v[110:113], v[30:33], v[102:105], v[110:113]
	v_mfma_f32_16x16x32_bf16 v[30:33], v[30:33], v[118:121], v[46:49]
	ds_read_b128 v[42:45], v244
	s_nop 1
	ds_read_b128 v[46:49], v244 offset:4096
	v_mfma_f32_16x16x32_bf16 v[114:117], v[34:37], v[102:105], v[114:117]
	v_mfma_f32_16x16x32_bf16 v[98:101], v[38:41], v[102:105], v[98:101]
	v_mfma_f32_16x16x32_bf16 v[34:37], v[34:37], v[118:121], v[50:53]
	v_mfma_f32_16x16x32_bf16 v[38:41], v[38:41], v[118:121], v[54:57]
	s_waitcnt lgkmcnt(1)
	v_mfma_f32_16x16x32_bf16 v[50:53], v[10:13], v[42:45], v[66:69]
	v_mfma_f32_16x16x32_bf16 v[54:57], v[14:17], v[42:45], v[70:73]
	v_mfma_f32_16x16x32_bf16 v[66:69], v[18:21], v[42:45], v[74:77]
	s_waitcnt vmcnt(1)
	v_mfma_f32_16x16x32_bf16 v[42:45], v[22:25], v[42:45], v[58:61]
	s_waitcnt lgkmcnt(0)
	v_mfma_f32_16x16x32_bf16 v[58:61], v[10:13], v[46:49], v[86:89]
	v_mfma_f32_16x16x32_bf16 v[70:73], v[14:17], v[46:49], v[90:93]
	v_mfma_f32_16x16x32_bf16 v[74:77], v[18:21], v[46:49], v[94:97]
	v_mfma_f32_16x16x32_bf16 v[46:49], v[22:25], v[46:49], v[62:65]
	s_nop 2
	ds_read_b128 v[62:65], v244 offset:8192
	ds_read_b128 v[86:89], v244 offset:12288
	s_waitcnt lgkmcnt(1)
	v_mfma_f32_16x16x32_bf16 v[114:117], v[18:21], v[62:65], v[114:117]
	s_waitcnt lgkmcnt(0)
	v_mfma_f32_16x16x32_bf16 v[176:179], v[18:21], v[86:89], v[34:37]
	v_add_u32_e32 v18, s53, v196
	v_add_u32_e32 v241, v18, v193
	s_ashr_i32 s53, s52, 31
	v_mfma_f32_16x16x32_bf16 v[90:93], v[10:13], v[62:65], v[106:109]
	s_lshl_b64 s[52:53], s[52:53], 16
	v_mfma_f32_16x16x32_bf16 v[110:113], v[14:17], v[62:65], v[110:113]
	v_mfma_f32_16x16x32_bf16 v[62:65], v[22:25], v[62:65], v[98:101]
	v_mfma_f32_16x16x32_bf16 v[180:183], v[22:25], v[86:89], v[38:41]
	ds_read_b128 v[18:21], v241
	ds_read_b128 v[22:25], v241 offset:4096
	s_waitcnt lgkmcnt(1)
	v_mfma_f32_16x16x32_bf16 v[150:153], v[2:5], v[18:21], v[50:53]
	v_mfma_f32_16x16x32_bf16 v[146:149], v[6:9], v[18:21], v[54:57]
	v_mfma_f32_16x16x32_bf16 v[106:109], v[78:81], v[18:21], v[66:69]
	s_waitcnt vmcnt(0)
	v_mfma_f32_16x16x32_bf16 v[102:105], v[82:85], v[18:21], v[42:45]
	ds_read_b128 v[18:21], v241 offset:8192
	ds_read_b128 v[246:249], v241 offset:12288
	s_waitcnt lgkmcnt(2)
	v_mfma_f32_16x16x32_bf16 v[142:145], v[2:5], v[22:25], v[58:61]
	v_mfma_f32_16x16x32_bf16 v[138:141], v[6:9], v[22:25], v[70:73]
	v_mfma_f32_16x16x32_bf16 v[98:101], v[78:81], v[22:25], v[74:77]
	v_mfma_f32_16x16x32_bf16 v[94:97], v[82:85], v[22:25], v[46:49]
	v_add_u32_e32 v22, s48, v159
	v_ashrrev_i32_e32 v23, 31, v22
	v_lshlrev_b64 v[24:25], 2, v[22:23]
	v_lshl_add_u64 v[174:175], s[12:13], 0, v[24:25]
	s_waitcnt lgkmcnt(1)
	v_mfma_f32_16x16x32_bf16 v[134:137], v[2:5], v[18:21], v[90:93]
	v_lshl_add_u64 v[172:173], s[16:17], 0, v[24:25]
	v_add_u32_e32 v22, 16, v22
	v_ashrrev_i32_e32 v23, 31, v22
	v_mfma_f32_16x16x32_bf16 v[90:93], v[78:81], v[18:21], v[114:117]
	global_load_dwordx4 v[118:121], v[174:175], off
	global_load_dwordx4 v[74:77], v[174:175], off offset:64
	s_nop 0
	global_load_dwordx4 v[114:117], v[172:173], off
	global_load_dwordx4 v[70:73], v[172:173], off offset:64
	v_lshl_add_u64 v[168:169], s[18:19], 0, v[24:25]
	s_waitcnt vmcnt(3)
	v_pk_add_f32 v[150:151], v[118:119], v[150:151]
	v_mfma_f32_16x16x32_bf16 v[10:13], v[10:13], v[86:89], v[26:29]
	s_waitcnt vmcnt(1)
	v_pk_add_f32 v[146:147], v[114:115], v[146:147]
	v_pk_mul_f32 v[150:151], v[150:151], s[44:45] op_sel_hi:[1,0]
	v_pk_mul_f32 v[146:147], v[146:147], s[44:45] op_sel_hi:[1,0]
	v_mfma_f32_16x16x32_bf16 v[14:17], v[14:17], v[86:89], v[30:33]
	v_exp_f32_e32 v150, v150
	v_exp_f32_e32 v151, v151
	s_waitcnt lgkmcnt(0)
	v_mfma_f32_16x16x32_bf16 v[126:129], v[2:5], v[246:249], v[10:13]
	v_lshl_add_u64 v[2:3], v[22:23], 2, s[18:19]
	s_nop 1
	v_lshl_add_u64 v[10:11], v[156:157], 0, s[52:53]
	v_add_co_u32_e32 v12, vcc, s3, v10
	v_mfma_f32_16x16x32_bf16 v[130:133], v[6:9], v[18:21], v[110:113]
	s_nop 0
	v_addc_co_u32_e32 v13, vcc, 0, v11, vcc
	s_nop 0
	global_load_dwordx4 v[110:113], v[168:169], off
	global_load_dwordx4 v[66:69], v[2:3], off
	v_mfma_f32_16x16x32_bf16 v[122:125], v[6:9], v[246:249], v[14:17]
	v_add_co_u32_e32 v6, vcc, s29, v10
	s_nop 1
	v_addc_co_u32_e32 v7, vcc, 0, v11, vcc
	v_mfma_f32_16x16x32_bf16 v[86:89], v[82:85], v[18:21], v[62:65]
	global_load_dwordx4 v[46:49], v[10:11], off
	global_load_dwordx4 v[30:33], v[10:11], off offset:1024
	global_load_dwordx4 v[18:21], v[10:11], off offset:2048
	global_load_dwordx4 v[2:5], v[10:11], off offset:3072
	global_load_dwordx4 v[38:41], v[12:13], off offset:1024
	global_load_dwordx4 v[22:25], v[12:13], off offset:2048
	global_load_dwordx4 v[54:57], v[6:7], off offset:-4096
	global_load_dwordx4 v[58:61], v[6:7], off
	global_load_dwordx4 v[42:45], v[6:7], off offset:1024
	global_load_dwordx4 v[26:29], v[6:7], off offset:2048
	s_nop 0
	global_load_dwordx4 v[6:9], v[6:7], off offset:3072
	v_add_co_u32_e32 v10, vcc, s47, v10
	v_mfma_f32_16x16x32_bf16 v[78:81], v[78:81], v[246:249], v[176:179]
	s_nop 0
	v_addc_co_u32_e32 v11, vcc, 0, v11, vcc
	global_load_dwordx4 v[14:17], v[12:13], off offset:3072
	global_load_dwordx4 v[62:65], v[10:11], off
	global_load_dwordx4 v[50:53], v[10:11], off offset:1024
	global_load_dwordx4 v[34:37], v[10:11], off offset:2048
	s_nop 0
	global_load_dwordx4 v[10:13], v[10:11], off offset:3072
	v_exp_f32_e32 v176, v146
	v_exp_f32_e32 v177, v147
	v_pk_add_f32 v[146:147], v[150:151], 1.0 op_sel_hi:[1,0]
	v_mfma_f32_16x16x32_bf16 v[82:85], v[82:85], v[246:249], v[180:183]
	v_add_f32_e64 v176, v176, 1.0
	v_add_f32_e64 v177, v177, 1.0
	v_pk_mul_f32 v[150:151], v[146:147], v[176:177]
	s_nop 0
	v_rcp_f32_e32 v178, v150
	v_rcp_f32_e32 v179, v151
	v_add_u32_e32 v150, v245, v197
	v_add_u32_e32 v154, v150, v198
	ds_read_b64 v[150:151], v154
	v_pk_mul_f32 v[176:177], v[176:177], v[178:179]
	s_waitcnt vmcnt(17)
	v_pk_mul_f32 v[176:177], v[110:111], v[176:177]
	s_nop 0
	v_pk_add_f32 v[182:183], v[176:177], v[176:177]
	s_nop 0
	v_pk_fma_f32 v[180:181], v[182:183], s[46:47], v[164:165] op_sel_hi:[1,0,0]
	v_min_f32_e32 v170, v182, v183
	v_pk_fma_f32 v[180:181], v[182:183], v[180:181], 0.5 op_sel_hi:[1,1,0]
	v_cmp_ge_f32_e32 vcc, s66, v170
	v_pk_fma_f32 v[180:181], v[182:183], v[180:181], 1.0 op_sel_hi:[1,1,0]
	s_nop 0
	v_pk_mul_f32 v[180:181], v[180:181], v[182:183] neg_lo:[0,1] neg_hi:[0,1]
	s_and_saveexec_b64 s[52:53], vcc
	s_cbranch_execnz .LBB0_1308

.LBB0_2155:
	s_cmp_lt_i32 s74, 18
	s_cselect_b64 s[0:1], -1, 0
	s_sub_i32 s30, s30, s33
	s_and_b64 s[8:9], s[0:1], s[6:7]
	s_andn2_b64 vcc, exec, s[8:9]
	s_lshl_b32 s6, s30, 2
	s_cbranch_vccnz .LBB0_2196
	s_cmp_gt_i32 s28, s6
	s_cselect_b64 s[0:1], -1, 0
	s_cmp_lt_i32 s2, s6
	s_cselect_b64 s[10:11], -1, 0
	s_cmp_ge_i32 s2, s6
	s_cselect_b64 s[4:5], -1, 0
	s_and_b64 s[4:5], s[0:1], s[4:5]
	s_mov_b64 s[0:1], -1
	s_and_b64 vcc, exec, s[4:5]
	s_cbranch_vccz .LBB0_2171
	s_sub_i32 s0, s28, s6
	s_lshl_b32 s0, s0, 3
	v_cvt_f32_u32_e32 v1, s0
	v_readlane_b32 s4, v254, 6
	v_readlane_b32 s5, v254, 7
	s_sub_i32 s5, 0, s0
	v_rcp_iflag_f32_e32 v1, v1
	s_sub_i32 s1, s2, s6
	s_lshl_b32 s1, s1, 3
	s_add_i32 s1, s1, s4
	v_mul_f32_e32 v1, 0x4f7ffffe, v1
	v_cvt_u32_f32_e32 v1, v1
	s_add_i32 s4, s0, 0x7fff
	v_readfirstlane_b32 s7, v1
	s_mul_i32 s5, s5, s7
	s_mul_hi_u32 s5, s7, s5
	s_add_i32 s7, s7, s5
	s_mul_hi_u32 s5, s4, s7
	s_mul_i32 s7, s5, s0
	s_sub_i32 s4, s4, s7
	s_add_i32 s12, s5, 1
	s_sub_i32 s7, s4, s0
	s_cmp_ge_u32 s4, s0
	s_cselect_b32 s5, s12, s5
	s_cselect_b32 s4, s7, s4
	s_add_i32 s7, s5, 1
	s_cmp_ge_u32 s4, s0
	s_cselect_b32 s4, s7, s5
	s_add_i32 s4, s4, 1
	s_and_b32 s0, s4, 0x7ffffffe
	s_mul_i32 s12, s0, s1
	s_add_i32 s0, s12, s0
	s_min_i32 s7, s0, 0x8000
	s_cmp_ge_u32 s12, s7
	s_mov_b32 s0, 0
	s_cbranch_scc1 .LBB0_2170
	s_waitcnt vmcnt(0)
	v_lshlrev_b32_e32 v18, 4, v250
	s_waitcnt lgkmcnt(0)
	global_load_dwordx4 v[2:5], v18, s[68:69]
	global_load_dwordx4 v[6:9], v18, s[68:69] offset:1024
	global_load_dwordx4 v[10:13], v18, s[68:69] offset:2048
	global_load_dwordx4 v[14:17], v18, s[68:69] offset:3072
	s_lshl_b32 s24, s31, 14
	s_add_u32 s25, s72, 0x180000
	s_addc_u32 s26, s73, 0
	s_add_u32 s27, s72, 0x140000
	v_lshlrev_b32_e32 v34, 2, v250
	v_mov_b32_e32 v35, 0
	s_addc_u32 s34, s73, 0
	s_lshr_b32 s4, s4, 1
	v_lshl_add_u64 v[26:27], s[72:73], 0, v[34:35]
	s_mov_b64 s[14:15], 0xdd00000
	s_mul_i32 s1, s1, s4
	s_ashr_i32 s13, s12, 31
	v_lshl_add_u64 v[36:37], v[26:27], 0, s[14:15]
	s_lshl_b32 s14, s1, 2
	s_lshl_b64 s[4:5], s[12:13], 11
	s_add_u32 s4, s72, s4
	v_lshlrev_b32_e32 v26, 3, v250
	v_mov_b32_e32 v27, v35
	s_addc_u32 s5, s73, s5
	v_lshl_add_u64 v[26:27], s[4:5], 0, v[26:27]
	s_mov_b64 s[4:5], 0x8c00e00
	v_lshl_add_u64 v[38:39], v[26:27], 0, s[4:5]
	s_lshl_b64 s[4:5], s[12:13], 12
	s_add_u32 s4, s70, s4
	v_mov_b32_e32 v19, v35
	s_addc_u32 s5, s71, s5
	v_or_b32_e32 v20, 0x100, v34
	v_or_b32_e32 v22, 0x200, v34
	v_or_b32_e32 v24, 0x300, v34
	v_lshl_add_u64 v[18:19], s[4:5], 0, v[18:19]
	s_mov_b64 s[16:17], 0x1000
	s_mov_b32 s1, s0
	v_lshl_add_u64 v[40:41], v[18:19], 0, s[16:17]
	s_mov_b32 s36, -1
	v_mov_b64_e32 v[42:43], s[0:1]
	s_add_i32 s13, 0, 0x20100
	v_lshlrev_b32_e32 v1, 2, v34
	v_lshlrev_b32_e32 v34, 2, v20
	v_lshlrev_b32_e32 v66, 2, v22
	v_lshlrev_b32_e32 v67, 2, v24
	v_mov_b32_e32 v68, 0x358637bd
	s_mov_b32 s35, 0x800000
	s_mov_b64 s[18:19], 0x2000
	v_mbcnt_lo_u32_b32 v69, -1, 0
	v_mov_b64_e32 v[44:45], s[0:1]
	v_mov_b32_e32 v18, 0
	v_mov_b32_e32 v19, v35
	v_mov_b32_e32 v20, v35
	v_mov_b32_e32 v21, v35
	v_mov_b32_e32 v22, v35
	v_mov_b32_e32 v23, v35
	v_mov_b32_e32 v24, v35
	v_mov_b32_e32 v25, v35
	v_mov_b32_e32 v26, v35
	v_mov_b32_e32 v27, v35
	v_mov_b32_e32 v28, v35
	v_mov_b32_e32 v29, v35
	v_mov_b32_e32 v30, v35
	v_mov_b32_e32 v31, v35
	v_mov_b32_e32 v32, v35
	v_mov_b32_e32 v33, v35
	v_lshlrev_b32_e32 v248, 2, v250
	s_ashr_i32 s15, s14, 31
	s_lshl_b64 s[98:99], s[14:15], 2
	s_add_u32 s98, s25, s98
	s_addc_u32 s99, s26, s99
	global_load_dword v249, v248, s[98:99]
	s_mov_b32 s100, 0
	s_waitcnt vmcnt(0)
	s_branch .LBB0_2160
.LBB0_2159:
	s_add_i32 s12, s12, 2
	s_add_i32 s14, s14, 4
	s_add_i32 s100, s100, 4
	v_lshl_add_u64 v[38:39], v[38:39], 0, s[16:17]
	s_cmp_lt_i32 s12, s7
	v_lshl_add_u64 v[40:41], v[40:41], 0, s[18:19]
	s_cbranch_scc0 .LBB0_2170
.LBB0_2160:
	s_ashr_i32 s15, s14, 31
	s_lshl_b64 s[0:1], s[14:15], 2
	s_add_u32 s4, s25, s0
	s_addc_u32 s5, s26, s1
	v_readlane_b32 s98, v249, s100
	s_add_i32 s4, s14, 1
	s_ashr_i32 s5, s4, 31
	s_lshl_b64 s[20:21], s[4:5], 2
	s_add_u32 s4, s25, s20
	s_addc_u32 s5, s26, s21
	s_add_i32 s101, s100, 1
	v_readlane_b32 s99, v249, s101
	s_nop 1
	v_mov_b32_e32 v62, s98
	v_mov_b32_e32 v63, s99
	s_waitcnt vmcnt(1)
	v_ashrrev_i32_e32 v64, 15, v62
	v_lshlrev_b32_e32 v64, 2, v64
	v_add_u32_e32 v64, s13, v64
	ds_read_b32 v64, v64
	v_and_b32_e32 v62, 0x7fff, v62
	s_waitcnt vmcnt(0)
	v_ashrrev_i32_e32 v65, 15, v63
	v_lshlrev_b32_e32 v65, 2, v65
	v_add_u32_e32 v65, s13, v65
	ds_read_b32 v65, v65
	s_waitcnt lgkmcnt(1)
	v_lshlrev_b32_e32 v64, 8, v64
	v_add_u32_e32 v64, v64, v62
	v_and_b32_e32 v63, 0x7fff, v63
	s_waitcnt lgkmcnt(0)
	v_lshlrev_b32_e32 v62, 8, v65
	v_add_u32_e32 v62, v62, v63
	v_max_i32_e32 v63, v64, v62
	v_cmp_gt_i32_e64 s[4:5], s24, v63
	s_and_b64 vcc, exec, s[4:5]
	s_cbranch_vccz .LBB0_2162
	s_add_u32 s0, s27, s0
	v_ashrrev_i32_e32 v65, 31, v64
	s_addc_u32 s1, s34, s1
	v_lshlrev_b64 v[52:53], 10, v[64:65]
	v_ashrrev_i32_e32 v63, 31, v62
	s_add_u32 s20, s27, s20
	v_lshl_add_u64 v[64:65], v[36:37], 0, v[52:53]
	v_lshlrev_b64 v[52:53], 10, v[62:63]
	s_addc_u32 s21, s34, s21
	global_load_dword v42, v35, s[0:1]
	global_load_dword v44, v35, s[20:21]
	v_lshl_add_u64 v[62:63], v[36:37], 0, v[52:53]
	global_load_dwordx2 v[52:53], v[38:39], off offset:-3584
	global_load_dwordx2 v[56:57], v[38:39], off offset:-3072
	global_load_dwordx2 v[58:59], v[38:39], off offset:-2560
	global_load_dwordx2 v[60:61], v[38:39], off offset:-2048
	global_load_dword v73, v[64:65], off
	global_load_dword v82, v[62:63], off
	global_load_dword v75, v[64:65], off offset:256
	global_load_dword v83, v[62:63], off offset:256
	global_load_dword v76, v[64:65], off offset:512
	global_load_dword v84, v[62:63], off offset:512
	global_load_dword v85, v[62:63], off offset:768
	global_load_dword v78, v[64:65], off offset:768
	s_waitcnt vmcnt(13)
	v_mul_f32_e32 v42, 0x3d800000, v42
	s_waitcnt vmcnt(12)
	v_mul_f32_e32 v44, 0x3d800000, v44
.LBB0_2162:
	s_add_i32 s0, s14, 2
	s_ashr_i32 s1, s0, 31
	s_lshl_b64 s[20:21], s[0:1], 2
	s_add_u32 s0, s25, s20
	s_addc_u32 s1, s26, s21
	s_add_i32 s101, s100, 2
	v_readlane_b32 s98, v249, s101
	s_add_i32 s0, s14, 3
	s_ashr_i32 s1, s0, 31
	s_lshl_b64 s[22:23], s[0:1], 2
	s_add_u32 s0, s25, s22
	s_addc_u32 s1, s26, s23
	s_add_i32 s101, s100, 3
	v_readlane_b32 s99, v249, s101
	s_nop 1
	v_mov_b32_e32 v62, s98
	v_mov_b32_e32 v63, s99
	s_waitcnt vmcnt(1)
	v_ashrrev_i32_e32 v64, 15, v62
	v_lshlrev_b32_e32 v64, 2, v64
	v_add_u32_e32 v64, s13, v64
	ds_read_b32 v64, v64
	v_and_b32_e32 v62, 0x7fff, v62
	s_waitcnt vmcnt(0)
	v_ashrrev_i32_e32 v65, 15, v63
	v_lshlrev_b32_e32 v65, 2, v65
	v_add_u32_e32 v65, s13, v65
	ds_read_b32 v65, v65
	s_waitcnt lgkmcnt(1)
	v_lshlrev_b32_e32 v64, 8, v64
	v_add_u32_e32 v64, v64, v62
	v_and_b32_e32 v63, 0x7fff, v63
	s_waitcnt lgkmcnt(0)
	v_lshlrev_b32_e32 v62, 8, v65
	v_add_u32_e32 v62, v62, v63
	v_max_i32_e32 v63, v64, v62
	v_cmp_le_i32_e32 vcc, s24, v63
	v_cmp_gt_i32_e64 s[0:1], s24, v63
	s_cbranch_vccnz .LBB0_2164
	s_add_u32 s20, s27, s20
	v_ashrrev_i32_e32 v65, 31, v64
	s_addc_u32 s21, s34, s21
	v_lshlrev_b64 v[46:47], 10, v[64:65]
	v_ashrrev_i32_e32 v63, 31, v62
	s_add_u32 s22, s27, s22
	v_lshl_add_u64 v[64:65], v[36:37], 0, v[46:47]
	v_lshlrev_b64 v[46:47], 10, v[62:63]
	s_addc_u32 s23, s34, s23
	global_load_dword v43, v35, s[20:21]
	global_load_dword v45, v35, s[22:23]
	v_lshl_add_u64 v[62:63], v[36:37], 0, v[46:47]
	global_load_dwordx2 v[46:47], v[38:39], off offset:-1536
	global_load_dwordx2 v[48:49], v[38:39], off offset:-1024
	global_load_dwordx2 v[50:51], v[38:39], off offset:-512
	global_load_dwordx2 v[54:55], v[38:39], off
	global_load_dword v70, v[64:65], off
	global_load_dword v77, v[62:63], off
	global_load_dword v71, v[64:65], off offset:256
	global_load_dword v79, v[62:63], off offset:256
	global_load_dword v72, v[64:65], off offset:512
	global_load_dword v80, v[62:63], off offset:512
	global_load_dword v81, v[62:63], off offset:768
	global_load_dword v74, v[64:65], off offset:768
	s_waitcnt vmcnt(13)
	v_mul_f32_e32 v43, 0x3d800000, v43
	s_waitcnt vmcnt(12)
	v_mul_f32_e32 v45, 0x3d800000, v45
